# speedup vs baseline: 1.0030x; 1.0015x over previous
.LBB2_12:
	s_add_i32 s16, s22, 0xffffc000
	s_and_b32 s16, s16, 0xc000
	v_add_u32_e32 v116, s16, v108
	s_add_u32 s16, s12, 0xfffce000
	s_addc_u32 s17, s13, -1
	v_readfirstlane_b32 s26, v116
	v_lshl_add_u64 v[116:117], s[16:17], 0, v[84:85]
	s_mov_b32 s27, m0
	s_mov_b32 m0, s26
	s_nop 0
	global_load_lds_dwordx4 v[116:117], off
	s_mov_b32 m0, s27
	v_lshl_add_u64 v[116:117], s[16:17], 0, v[86:87]
	s_add_i32 s16, s26, 0x400
	s_mov_b32 s17, m0
	s_mov_b32 m0, s16
	s_nop 0
	global_load_lds_dwordx4 v[116:117], off
	s_mov_b32 m0, s17
	s_and_b32 s16, s22, 0xc000
	v_add_u32_e32 v116, s16, v108
	s_nop 0
	v_readfirstlane_b32 s16, v116
	v_lshl_add_u64 v[116:117], s[12:13], 0, v[84:85]
	s_mov_b32 s17, m0
	s_mov_b32 m0, s16
	s_nop 0
	global_load_lds_dwordx4 v[116:117], off
	s_mov_b32 m0, s17
	v_lshl_add_u64 v[116:117], s[12:13], 0, v[86:87]
	s_addk_i32 s16, 0x400
	s_mov_b32 s17, m0
	s_mov_b32 m0, s16
	s_nop 0
	global_load_lds_dwordx4 v[116:117], off
	s_mov_b32 m0, s17
	v_cmp_neq_f32_e32 vcc, s25, v102
	v_add_u32_e32 v114, v114, v98
	v_add_u32_e32 v107, 2, v107
	v_cndmask_b32_e64 v124, v112, -v102, vcc
	v_fmamk_f32 v34, v34, 0x3e38aa3b, v124
	v_fmamk_f32 v50, v50, 0x3e38aa3b, v124
	v_exp_f32_e32 v126, v34
	v_fmamk_f32 v34, v51, 0x3e38aa3b, v124
	v_exp_f32_e32 v125, v50
	v_exp_f32_e32 v82, v34
	v_fmamk_f32 v34, v35, 0x3e38aa3b, v124
	v_exp_f32_e32 v34, v34
	v_add_f32_e32 v35, v126, v125
	v_fmamk_f32 v36, v36, 0x3e38aa3b, v124
	v_exp_f32_e32 v127, v36
	v_pk_add_f32 v[50:51], v[34:35], v[82:83]
	v_fmamk_f32 v35, v52, 0x3e38aa3b, v124
	v_pk_add_f32 v[88:89], v[50:51], v[50:51] op_sel_hi:[0,1]
	v_fmamk_f32 v36, v53, 0x3e38aa3b, v124
	v_exp_f32_e32 v35, v35
	v_exp_f32_e32 v88, v36
	v_fmamk_f32 v36, v37, 0x3e38aa3b, v124
	v_exp_f32_e32 v36, v36
	v_add_f32_e32 v37, v127, v35
	v_fmamk_f32 v38, v38, 0x3e38aa3b, v124
	v_exp_f32_e32 v115, v38
	v_pk_add_f32 v[50:51], v[36:37], v[88:89]
	v_fmamk_f32 v37, v54, 0x3e38aa3b, v124
	v_pk_add_f32 v[90:91], v[50:51], v[50:51] op_sel_hi:[0,1]
	v_fmamk_f32 v38, v55, 0x3e38aa3b, v124
	v_exp_f32_e32 v37, v37
	v_exp_f32_e32 v90, v38
	v_fmamk_f32 v38, v39, 0x3e38aa3b, v124
	v_exp_f32_e32 v50, v38
	v_add_f32_e32 v51, v115, v37
	s_add_u32 s12, s12, 0x64000
	s_addc_u32 s13, s13, 0
	v_pk_add_f32 v[38:39], v[50:51], v[90:91]
	s_add_i32 s22, s22, 0x8000
	v_pk_add_f32 v[54:55], v[38:39], v[38:39] op_sel_hi:[0,1]
	v_fmamk_f32 v38, v56, 0x3e38aa3b, v124
	v_exp_f32_e32 v51, v38
	v_fmamk_f32 v38, v40, 0x3e38aa3b, v124
	v_exp_f32_e32 v91, v38
	v_fmamk_f32 v38, v57, 0x3e38aa3b, v124
	v_exp_f32_e32 v54, v38
	v_fmamk_f32 v38, v41, 0x3e38aa3b, v124
	v_exp_f32_e32 v52, v38
	v_add_f32_e32 v53, v91, v51
	v_cvt_pk_f16_f32 v57, v51, v54
	v_cvt_pk_f16_f32 v56, v37, v90
	v_pk_add_f32 v[38:39], v[52:53], v[54:55]
	v_cvt_pk_f16_f32 v55, v35, v88
	v_pk_add_f32 v[116:117], v[38:39], v[38:39] op_sel_hi:[0,1]
	v_fmamk_f32 v38, v58, 0x3e38aa3b, v124
	v_exp_f32_e32 v53, v38
	v_fmamk_f32 v38, v42, 0x3e38aa3b, v124
	v_exp_f32_e32 v1, v38
	v_fmamk_f32 v38, v59, 0x3e38aa3b, v124
	v_exp_f32_e32 v116, v38
	v_fmamk_f32 v38, v43, 0x3e38aa3b, v124
	v_exp_f32_e32 v38, v38
	v_add_f32_e32 v39, v1, v53
	v_cvt_pk_f16_f32 v54, v125, v82
	v_fmamk_f32 v35, v64, 0x3e38aa3b, v124
	v_pk_add_f32 v[40:41], v[38:39], v[116:117]
	v_fmamk_f32 v39, v60, 0x3e38aa3b, v124
	v_pk_add_f32 v[118:119], v[40:41], v[40:41] op_sel_hi:[0,1]
	v_fmamk_f32 v40, v44, 0x3e38aa3b, v124
	v_exp_f32_e32 v117, v40
	v_fmamk_f32 v40, v61, 0x3e38aa3b, v124
	ds_read_b64_tr_b16 v[58:59], v114 offset:9216
	ds_read_b64_tr_b16 v[60:61], v114 offset:9728
	v_exp_f32_e32 v39, v39
	v_exp_f32_e32 v118, v40
	v_fmamk_f32 v40, v45, 0x3e38aa3b, v124
	ds_read_b64_tr_b16 v[44:45], v114 offset:8704
	v_exp_f32_e32 v40, v40
	v_add_f32_e32 v41, v117, v39
	v_exp_f32_e32 v82, v35
	v_fmamk_f32 v35, v65, 0x3e38aa3b, v124
	v_pk_add_f32 v[42:43], v[40:41], v[118:119]
	v_fmamk_f32 v41, v62, 0x3e38aa3b, v124
	v_pk_add_f32 v[120:121], v[42:43], v[42:43] op_sel_hi:[0,1]
	v_fmamk_f32 v42, v46, 0x3e38aa3b, v124
	v_exp_f32_e32 v119, v42
	v_fmamk_f32 v42, v63, 0x3e38aa3b, v124
	ds_read_b64_tr_b16 v[62:63], v114 offset:13312
	ds_read_b64_tr_b16 v[64:65], v114 offset:13824
	v_exp_f32_e32 v41, v41
	v_exp_f32_e32 v120, v42
	v_fmamk_f32 v42, v47, 0x3e38aa3b, v124
	v_exp_f32_e32 v122, v42
	ds_read_b64_tr_b16 v[42:43], v114 offset:8192
	v_add_f32_e32 v123, v119, v41
	v_pk_add_f32 v[46:47], v[122:123], v[120:121]
	s_waitcnt lgkmcnt(0)
	v_mfma_f32_32x32x16_f16 v[18:33], v[54:57], v[42:45], v[18:33]
	v_add_f32_e64 v88, v46, v46
	v_add_f32_e64 v89, v46, v47
	ds_read_b64_tr_b16 v[42:43], v114 offset:12288
	ds_read_b64_tr_b16 v[44:45], v114 offset:12800
	v_exp_f32_e32 v88, v35
	v_cvt_pk_f16_f32 v51, v127, v36
	v_cmp_le_u32_e32 vcc, s21, v107
	s_or_b64 s[14:15], vcc, s[14:15]
	s_waitcnt lgkmcnt(0)
	v_mfma_f32_32x32x16_f16 v[2:17], v[54:57], v[42:45], v[2:17]
	v_cvt_pk_f16_f32 v45, v82, v88
	v_cvt_pk_f16_f32 v44, v41, v120
	v_cvt_pk_f16_f32 v43, v39, v118
	v_cvt_pk_f16_f32 v42, v53, v116
	v_cvt_pk_f16_f32 v53, v91, v52
	v_cvt_pk_f16_f32 v52, v115, v50
	v_cvt_pk_f16_f32 v50, v126, v34
	v_mfma_f32_32x32x16_f16 v[18:33], v[42:45], v[58:61], v[18:33]
	v_fmamk_f32 v39, v48, 0x3e38aa3b, v124
	v_fmac_f32_e32 v124, 0x3e38aa3b, v49
	v_exp_f32_e32 v39, v39
	v_exp_f32_e32 v54, v124
	v_cvt_pk_f16_f32 v41, v117, v40
	v_cvt_pk_f16_f32 v40, v1, v38
	v_add_f32_e32 v55, v39, v82
	s_waitcnt lgkmcnt(0)
	v_mfma_f32_32x32x16_f16 v[2:17], v[42:45], v[62:65], v[2:17]
	ds_read_b64_tr_b16 v[42:43], v114 offset:10240
	ds_read_b64_tr_b16 v[44:45], v114 offset:10752
	ds_read_b64_tr_b16 v[34:35], v114 offset:11264
	ds_read_b64_tr_b16 v[36:37], v114 offset:11776
	s_waitcnt lgkmcnt(2)
	v_mfma_f32_32x32x16_f16 v[18:33], v[50:53], v[42:45], v[18:33]
	ds_read_b64_tr_b16 v[42:43], v114 offset:14336
	ds_read_b64_tr_b16 v[44:45], v114 offset:14848
	ds_read_b64_tr_b16 v[46:47], v114 offset:15360
	ds_read_b64_tr_b16 v[48:49], v114 offset:15872
	s_waitcnt lgkmcnt(2)
	v_mfma_f32_32x32x16_f16 v[2:17], v[50:53], v[42:45], v[2:17]
	v_cvt_pk_f16_f32 v43, v39, v54
	v_cvt_pk_f16_f32 v42, v119, v122
	s_nop 1
	v_mfma_f32_32x32x16_f16 v[18:33], v[40:43], v[34:37], v[18:33]
	v_add_f32_e64 v34, v54, v88
	v_add_f32_e64 v35, v55, v89
	v_mov_b32_e32 v88, v102
	v_add_f32_e32 v1, v34, v35
	v_add_f32_e32 v113, v113, v1
	s_waitcnt lgkmcnt(0)
	v_mfma_f32_32x32x16_f16 v[2:17], v[40:43], v[46:49], v[2:17]
	s_andn2_b64 exec, exec, s[14:15]
	s_cbranch_execz .LBB2_17
